# adaLN partial sums: 12-step remainder loop unrolled by hand with all 12 row loads in flight (was load, wait, use x12)
# speedup vs baseline: 1.0079x; 1.0079x over previous
.LBB0_16:
	global_load_dwordx4 v[60:63], v[14:15], off
	ds_read2st64_b32 v[108:109], v16 offset1:8
	v_lshl_add_u64 v[14:15], v[14:15], 0, s[18:19]
	v_add_u32_e32 v16, 40, v16
	global_load_dwordx4 v[64:67], v[14:15], off
	ds_read2st64_b32 v[110:111], v16 offset1:8
	v_lshl_add_u64 v[14:15], v[14:15], 0, s[18:19]
	v_add_u32_e32 v16, 40, v16
	global_load_dwordx4 v[68:71], v[14:15], off
	ds_read2st64_b32 v[112:113], v16 offset1:8
	v_lshl_add_u64 v[14:15], v[14:15], 0, s[18:19]
	v_add_u32_e32 v16, 40, v16
	global_load_dwordx4 v[72:75], v[14:15], off
	ds_read2st64_b32 v[114:115], v16 offset1:8
	v_lshl_add_u64 v[14:15], v[14:15], 0, s[18:19]
	v_add_u32_e32 v16, 40, v16
	global_load_dwordx4 v[76:79], v[14:15], off
	ds_read2st64_b32 v[116:117], v16 offset1:8
	v_lshl_add_u64 v[14:15], v[14:15], 0, s[18:19]
	v_add_u32_e32 v16, 40, v16
	global_load_dwordx4 v[80:83], v[14:15], off
	ds_read2st64_b32 v[118:119], v16 offset1:8
	v_lshl_add_u64 v[14:15], v[14:15], 0, s[18:19]
	v_add_u32_e32 v16, 40, v16
	global_load_dwordx4 v[84:87], v[14:15], off
	ds_read2st64_b32 v[120:121], v16 offset1:8
	v_lshl_add_u64 v[14:15], v[14:15], 0, s[18:19]
	v_add_u32_e32 v16, 40, v16
	global_load_dwordx4 v[88:91], v[14:15], off
	ds_read2st64_b32 v[122:123], v16 offset1:8
	v_lshl_add_u64 v[14:15], v[14:15], 0, s[18:19]
	v_add_u32_e32 v16, 40, v16
	global_load_dwordx4 v[92:95], v[14:15], off
	ds_read2st64_b32 v[124:125], v16 offset1:8
	v_lshl_add_u64 v[14:15], v[14:15], 0, s[18:19]
	v_add_u32_e32 v16, 40, v16
	global_load_dwordx4 v[96:99], v[14:15], off
	ds_read2st64_b32 v[126:127], v16 offset1:8
	v_lshl_add_u64 v[14:15], v[14:15], 0, s[18:19]
	v_add_u32_e32 v16, 40, v16
	global_load_dwordx4 v[100:103], v[14:15], off
	ds_read2st64_b32 v[128:129], v16 offset1:8
	v_lshl_add_u64 v[14:15], v[14:15], 0, s[18:19]
	v_add_u32_e32 v16, 40, v16
	global_load_dwordx4 v[104:107], v[14:15], off
	ds_read2st64_b32 v[130:131], v16 offset1:8
	v_lshl_add_u64 v[14:15], v[14:15], 0, s[18:19]
	v_add_u32_e32 v16, 40, v16
	v_add_u32_e32 v38, 0x78, v38
	v_mov_b32_e32 v1, 0
	s_waitcnt lgkmcnt(0)
	s_waitcnt vmcnt(11)
	v_mov_b32_e32 v132, v109
	v_pk_fma_f32 v[4:5], v[62:63], v[108:109], v[4:5] op_sel_hi:[1,0,1]
	v_pk_fma_f32 v[2:3], v[60:61], v[108:109], v[2:3] op_sel_hi:[1,0,1]
	v_pk_fma_f32 v[8:9], v[62:63], v[132:133], v[8:9] op_sel_hi:[1,0,1]
	v_pk_fma_f32 v[6:7], v[60:61], v[132:133], v[6:7] op_sel_hi:[1,0,1]
	s_waitcnt vmcnt(10)
	v_mov_b32_e32 v132, v111
	v_pk_fma_f32 v[4:5], v[66:67], v[110:111], v[4:5] op_sel_hi:[1,0,1]
	v_pk_fma_f32 v[2:3], v[64:65], v[110:111], v[2:3] op_sel_hi:[1,0,1]
	v_pk_fma_f32 v[8:9], v[66:67], v[132:133], v[8:9] op_sel_hi:[1,0,1]
	v_pk_fma_f32 v[6:7], v[64:65], v[132:133], v[6:7] op_sel_hi:[1,0,1]
	s_waitcnt vmcnt(9)
	v_mov_b32_e32 v132, v113
	v_pk_fma_f32 v[4:5], v[70:71], v[112:113], v[4:5] op_sel_hi:[1,0,1]
	v_pk_fma_f32 v[2:3], v[68:69], v[112:113], v[2:3] op_sel_hi:[1,0,1]
	v_pk_fma_f32 v[8:9], v[70:71], v[132:133], v[8:9] op_sel_hi:[1,0,1]
	v_pk_fma_f32 v[6:7], v[68:69], v[132:133], v[6:7] op_sel_hi:[1,0,1]
	s_waitcnt vmcnt(8)
	v_mov_b32_e32 v132, v115
	v_pk_fma_f32 v[4:5], v[74:75], v[114:115], v[4:5] op_sel_hi:[1,0,1]
	v_pk_fma_f32 v[2:3], v[72:73], v[114:115], v[2:3] op_sel_hi:[1,0,1]
	v_pk_fma_f32 v[8:9], v[74:75], v[132:133], v[8:9] op_sel_hi:[1,0,1]
	v_pk_fma_f32 v[6:7], v[72:73], v[132:133], v[6:7] op_sel_hi:[1,0,1]
	s_waitcnt vmcnt(7)
	v_mov_b32_e32 v132, v117
	v_pk_fma_f32 v[4:5], v[78:79], v[116:117], v[4:5] op_sel_hi:[1,0,1]
	v_pk_fma_f32 v[2:3], v[76:77], v[116:117], v[2:3] op_sel_hi:[1,0,1]
	v_pk_fma_f32 v[8:9], v[78:79], v[132:133], v[8:9] op_sel_hi:[1,0,1]
	v_pk_fma_f32 v[6:7], v[76:77], v[132:133], v[6:7] op_sel_hi:[1,0,1]
	s_waitcnt vmcnt(6)
	v_mov_b32_e32 v132, v119
	v_pk_fma_f32 v[4:5], v[82:83], v[118:119], v[4:5] op_sel_hi:[1,0,1]
	v_pk_fma_f32 v[2:3], v[80:81], v[118:119], v[2:3] op_sel_hi:[1,0,1]
	v_pk_fma_f32 v[8:9], v[82:83], v[132:133], v[8:9] op_sel_hi:[1,0,1]
	v_pk_fma_f32 v[6:7], v[80:81], v[132:133], v[6:7] op_sel_hi:[1,0,1]
	s_waitcnt vmcnt(5)
	v_mov_b32_e32 v132, v121
	v_pk_fma_f32 v[4:5], v[86:87], v[120:121], v[4:5] op_sel_hi:[1,0,1]
	v_pk_fma_f32 v[2:3], v[84:85], v[120:121], v[2:3] op_sel_hi:[1,0,1]
	v_pk_fma_f32 v[8:9], v[86:87], v[132:133], v[8:9] op_sel_hi:[1,0,1]
	v_pk_fma_f32 v[6:7], v[84:85], v[132:133], v[6:7] op_sel_hi:[1,0,1]
	s_waitcnt vmcnt(4)
	v_mov_b32_e32 v132, v123
	v_pk_fma_f32 v[4:5], v[90:91], v[122:123], v[4:5] op_sel_hi:[1,0,1]
	v_pk_fma_f32 v[2:3], v[88:89], v[122:123], v[2:3] op_sel_hi:[1,0,1]
	v_pk_fma_f32 v[8:9], v[90:91], v[132:133], v[8:9] op_sel_hi:[1,0,1]
	v_pk_fma_f32 v[6:7], v[88:89], v[132:133], v[6:7] op_sel_hi:[1,0,1]
	s_waitcnt vmcnt(3)
	v_mov_b32_e32 v132, v125
	v_pk_fma_f32 v[4:5], v[94:95], v[124:125], v[4:5] op_sel_hi:[1,0,1]
	v_pk_fma_f32 v[2:3], v[92:93], v[124:125], v[2:3] op_sel_hi:[1,0,1]
	v_pk_fma_f32 v[8:9], v[94:95], v[132:133], v[8:9] op_sel_hi:[1,0,1]
	v_pk_fma_f32 v[6:7], v[92:93], v[132:133], v[6:7] op_sel_hi:[1,0,1]
	s_waitcnt vmcnt(2)
	v_mov_b32_e32 v132, v127
	v_pk_fma_f32 v[4:5], v[98:99], v[126:127], v[4:5] op_sel_hi:[1,0,1]
	v_pk_fma_f32 v[2:3], v[96:97], v[126:127], v[2:3] op_sel_hi:[1,0,1]
	v_pk_fma_f32 v[8:9], v[98:99], v[132:133], v[8:9] op_sel_hi:[1,0,1]
	v_pk_fma_f32 v[6:7], v[96:97], v[132:133], v[6:7] op_sel_hi:[1,0,1]
	s_waitcnt vmcnt(1)
	v_mov_b32_e32 v132, v129
	v_pk_fma_f32 v[4:5], v[102:103], v[128:129], v[4:5] op_sel_hi:[1,0,1]
	v_pk_fma_f32 v[2:3], v[100:101], v[128:129], v[2:3] op_sel_hi:[1,0,1]
	v_pk_fma_f32 v[8:9], v[102:103], v[132:133], v[8:9] op_sel_hi:[1,0,1]
	v_pk_fma_f32 v[6:7], v[100:101], v[132:133], v[6:7] op_sel_hi:[1,0,1]
	s_waitcnt vmcnt(0)
	v_mov_b32_e32 v132, v131
	v_pk_fma_f32 v[4:5], v[106:107], v[130:131], v[4:5] op_sel_hi:[1,0,1]
	v_pk_fma_f32 v[2:3], v[104:105], v[130:131], v[2:3] op_sel_hi:[1,0,1]
	v_pk_fma_f32 v[8:9], v[106:107], v[132:133], v[8:9] op_sel_hi:[1,0,1]
	v_pk_fma_f32 v[6:7], v[104:105], v[132:133], v[6:7] op_sel_hi:[1,0,1]
	s_or_b64 exec, exec, s[28:29]
